# peersel middle stage rewritten by hand: one pass, 4 lanes per row with 32 keys each (two sort16 + local merge + two cross-lane merges) instead of two passes of 8 lanes x 16 keys; same keys, same lists
# speedup vs baseline: 1.0203x; 1.0097x over previous
; #define MFMA16(a, b, c) __builtin_amdgcn_mfma_f32_16x16x32_bf16((a), (b), (c), 0, 0, 0)
; DI void peer_select_unit(const Params& p, int unit, char* lds, const bf16x8 (&kb)[4][4]) {
;     ...
;     const int set = wid >> 1, kh = wid & 1;
;     bf16x8 qa[2][4];
; #pragma unroll
;     for (int mt = 0; mt < 2; ++mt)
; #pragma unroll
;       for (int kk = 0; kk < 4; ++kk) qa[mt][kk] = *(const bf16x8*)(qy + (size_t)(t0 + 16 * mt + fr) * 2048 + h * 256 + set * 128 + kk * 32 + fq * 8);
; #pragma unroll
;     for (int mt = 0; mt < 2; ++mt)
; #pragma unroll
;       for (int nj = 0; nj < 4; ++nj) {
;         f32x4 d = {0.f, 0.f, 0.f, 0.f};
; #pragma unroll
;         for (int kk = 0; kk < 4; ++kk) d = MFMA16(qa[mt][kk], kb[nj][kk], d);
; #pragma unroll
;         for (int r = 0; r < 4; ++r) sc[(set * 32 + 16 * mt + 4 * fq + r) * 132 + 64 * kh + 16 * nj + fr] = d[r];
;       }
;   }
;   __syncthreads();
; #pragma unroll 1
;   for (int pass = 0; pass < 2; ++pass) {
;     const int rr = pass * 32 + (tid >> 3), part = tid & 7;
.LBB0_1652:
	v_lshlrev_b32_e32 v64, 2, v72
	v_mov_b32_e32 v66, v206
	v_and_b32_e32 v73, 7, v72
	v_and_b32_e32 v74, 0xffffffe0, v64
	v_lshlrev_b32_e32 v64, 9, v73
	v_and_or_b32 v84, v66, 15, v74
	v_and_b32_e32 v70, 0xffffff80, v66
	v_bfe_u32 v67, v66, 4, 2
	v_lshl_add_u64 v[68:69], s[58:59], 0, v[64:65]
	v_ashrrev_i32_e32 v71, 31, v70
	v_or_b32_e32 v90, 16, v84
	v_lshl_add_u64 v[68:69], v[70:71], 1, v[68:69]
	v_lshlrev_b32_e32 v64, 4, v67
	v_ashrrev_i32_e32 v85, 31, v84
	v_ashrrev_i32_e32 v91, 31, v90
	v_lshl_add_u64 v[88:89], v[68:69], 0, v[64:65]
	v_lshlrev_b64 v[68:69], 12, v[84:85]
	v_lshlrev_b64 v[90:91], 12, v[90:91]
	v_lshl_add_u64 v[116:117], v[88:89], 0, v[68:69]
	v_lshl_add_u64 v[120:121], v[88:89], 0, v[90:91]
	s_barrier
	s_waitcnt vmcnt(0)
	v_mov_b32_e32 v68, v148
	v_mov_b32_e32 v69, v149
	v_mov_b32_e32 v70, v150
	v_mov_b32_e32 v71, v151
	v_mov_b32_e32 v76, v152
	v_mov_b32_e32 v77, v153
	v_mov_b32_e32 v78, v154
	v_mov_b32_e32 v79, v155
	v_mov_b32_e32 v92, v156
	v_mov_b32_e32 v93, v157
	v_mov_b32_e32 v94, v158
	v_mov_b32_e32 v95, v159
	v_mov_b32_e32 v96, v160
	v_mov_b32_e32 v97, v161
	v_mov_b32_e32 v98, v162
	v_mov_b32_e32 v99, v163
	v_ashrrev_i32_e32 v75, 2, v66
	v_and_b32_e32 v64, 0x4f, v66
	v_lshlrev_b32_e32 v64, 2, v64
	s_mov_b64 s[20:21], -1
	s_mov_b32 s69, 0
	v_mfma_f32_16x16x32_bf16 v[80:83], v[68:71], v[0:3], 0
	v_mfma_f32_16x16x32_bf16 v[84:87], v[68:71], v[56:59], 0
	v_mfma_f32_16x16x32_bf16 v[88:91], v[68:71], v[24:27], 0
	v_mfma_f32_16x16x32_bf16 v[68:71], v[68:71], v[44:47], 0
	v_mfma_f32_16x16x32_bf16 v[100:103], v[92:95], v[0:3], 0
	v_mfma_f32_16x16x32_bf16 v[104:107], v[92:95], v[56:59], 0
	v_mfma_f32_16x16x32_bf16 v[108:111], v[92:95], v[24:27], 0
	v_mfma_f32_16x16x32_bf16 v[80:83], v[76:79], v[4:7], v[80:83]
	v_mfma_f32_16x16x32_bf16 v[84:87], v[76:79], v[16:19], v[84:87]
	v_mfma_f32_16x16x32_bf16 v[88:91], v[76:79], v[28:31], v[88:91]
	v_mfma_f32_16x16x32_bf16 v[68:71], v[76:79], v[48:51], v[68:71]
	v_mfma_f32_16x16x32_bf16 v[76:79], v[96:99], v[4:7], v[100:103]
	v_mfma_f32_16x16x32_bf16 v[100:103], v[96:99], v[16:19], v[104:107]
	v_mfma_f32_16x16x32_bf16 v[104:107], v[96:99], v[28:31], v[108:111]
	s_nop 2
	s_nop 1
	v_mov_b32_e32 v108, v164
	v_mov_b32_e32 v109, v165
	v_mov_b32_e32 v110, v166
	v_mov_b32_e32 v111, v167
	v_mov_b32_e32 v112, v168
	v_mov_b32_e32 v113, v169
	v_mov_b32_e32 v114, v170
	v_mov_b32_e32 v115, v171
	v_mov_b32_e32 v116, v172
	v_mov_b32_e32 v117, v173
	v_mov_b32_e32 v118, v174
	v_mov_b32_e32 v119, v175
	s_nop 1
	v_mfma_f32_16x16x32_bf16 v[80:83], v[108:111], v[8:11], v[80:83]
	v_mfma_f32_16x16x32_bf16 v[84:87], v[108:111], v[20:23], v[84:87]
	v_mfma_f32_16x16x32_bf16 v[88:91], v[108:111], v[32:35], v[88:91]
	v_mfma_f32_16x16x32_bf16 v[68:71], v[108:111], v[52:55], v[68:71]
	s_nop 3
	v_mov_b32_e32 v108, v178
	v_mov_b32_e32 v109, v179
	v_mov_b32_e32 v110, v180
	v_mov_b32_e32 v111, v181
	v_add_u32_e32 v184, s90, v72
	v_min_u32_e32 v184, s68, v184
	v_lshrrev_b32_e32 v185, 3, v184
	v_lshlrev_b32_e32 v185, 17, v185
	v_and_b32_e32 v184, 7, v184
	v_lshl_or_b32 v184, v184, 9, v185
	v_mov_b32_e32 v185, 0
	v_lshl_add_u64 v[184:185], v[182:183], 0, v[184:185]
	v_mov_b32_e32 v186, 0x10000
	v_mov_b32_e32 v187, 0
	v_lshl_add_u64 v[186:187], v[184:185], 0, v[186:187]
	global_load_dwordx4 v[148:151], v[184:185], off
	global_load_dwordx4 v[152:155], v[184:185], off offset:64
	global_load_dwordx4 v[156:159], v[186:187], off
	global_load_dwordx4 v[160:163], v[186:187], off offset:64
	global_load_dwordx4 v[164:167], v[184:185], off offset:128
	global_load_dwordx4 v[168:171], v[184:185], off offset:192
	global_load_dwordx4 v[172:175], v[186:187], off offset:128
	global_load_dwordx4 v[178:181], v[186:187], off offset:192
	s_nop 1
	v_mfma_f32_16x16x32_bf16 v[80:83], v[112:115], v[12:15], v[80:83]
	v_mfma_f32_16x16x32_bf16 v[84:87], v[112:115], v[40:43], v[84:87]
	v_mfma_f32_16x16x32_bf16 v[88:91], v[112:115], v[36:39], v[88:91]
	v_mfma_f32_16x16x32_bf16 v[68:71], v[112:115], v[60:63], v[68:71]
	v_and_b32_e32 v112, 0xfffffe0, v75
	v_lshl_or_b32 v67, v67, 2, v112
	v_mul_lo_u32 v67, v67, s2
	v_add3_u32 v64, v146, v67, v64
	v_add_u32_e32 v67, 0x400, v64
	s_nop 0
	ds_write2_b32 v64, v80, v84 offset1:16
	ds_write2_b32 v64, v81, v85 offset0:132 offset1:148
	ds_write2_b32 v67, v82, v86 offset0:8 offset1:24
	ds_write2_b32 v67, v83, v87 offset0:140 offset1:156
	ds_write2_b32 v64, v88, v68 offset0:32 offset1:48
	v_mfma_f32_16x16x32_bf16 v[80:83], v[92:95], v[44:47], 0
	ds_write2_b32 v64, v89, v69 offset0:164 offset1:180
	ds_write2_b32 v67, v90, v70 offset0:40 offset1:56
	ds_write2_b32 v67, v91, v71 offset0:172 offset1:188
	v_add_u32_e32 v67, 0x2000, v64
	v_add_u32_e32 v64, 0x2400, v64
	v_mfma_f32_16x16x32_bf16 v[68:71], v[96:99], v[48:51], v[80:83]
	v_mfma_f32_16x16x32_bf16 v[76:79], v[116:119], v[8:11], v[76:79]
	v_mfma_f32_16x16x32_bf16 v[100:103], v[116:119], v[20:23], v[100:103]
	v_mfma_f32_16x16x32_bf16 v[104:107], v[116:119], v[32:35], v[104:107]
	v_mfma_f32_16x16x32_bf16 v[68:71], v[116:119], v[52:55], v[68:71]
	v_mfma_f32_16x16x32_bf16 v[76:79], v[108:111], v[12:15], v[76:79]
	v_mfma_f32_16x16x32_bf16 v[100:103], v[108:111], v[40:43], v[100:103]
	s_nop 7
	ds_write2_b32 v67, v76, v100 offset0:64 offset1:80
	ds_write2_b32 v67, v77, v101 offset0:196 offset1:212
	v_mfma_f32_16x16x32_bf16 v[104:107], v[108:111], v[36:39], v[104:107]
	ds_write2_b32 v64, v78, v102 offset0:72 offset1:88
	ds_write2_b32 v64, v79, v103 offset0:204 offset1:220
	v_mfma_f32_16x16x32_bf16 v[68:71], v[108:111], v[60:63], v[68:71]
	s_nop 7
	ds_write2_b32 v67, v104, v68 offset0:96 offset1:112
	ds_write2_b32 v67, v105, v69 offset0:228 offset1:244
	ds_write2_b32 v64, v106, v70 offset0:104 offset1:120
	ds_write2_b32 v64, v107, v71 offset0:236 offset1:252
	v_lshrrev_b32_e32 v236, 2, v66
	v_and_b32_e32 v237, 3, v66
	v_mul_u32_u24_e32 v238, 0x210, v236
	v_add_u32_e32 v238, v146, v238
	v_lshl_add_u32 v239, v237, 6, v238
	s_waitcnt lgkmcnt(0)
	s_barrier
; DI unsigned ordkey(float f) { const unsigned u = __float_as_uint(f); return (u & 0x80000000u) ? ~u : (u | 0x80000000u); }
; DI void peer_select_unit(const Params& p, int unit, char* lds, const bf16x8 (&kb)[4][4]) {
;     ...
;     const float* srow = sc + rr * 132 + 16 * part;
; #pragma unroll
;     for (int j = 0; j < 4; ++j) {
;       const f32x4 v = *(const f32x4*)(srow + 4 * j);
; #pragma unroll
;       for (int e = 0; e < 4; ++e) a[4 * j + e] = (ordkey(v[e]) & ~127u) | (unsigned)(127 - (16 * part + 4 * j + e));
;     }
	ds_read_b128 v[124:127], v239 offset:0
	ds_read_b128 v[128:131], v239 offset:16
	ds_read_b128 v[132:135], v239 offset:32
	ds_read_b128 v[136:139], v239 offset:48
	ds_read_b128 v[212:215], v239 offset:256
	ds_read_b128 v[216:219], v239 offset:272
	ds_read_b128 v[220:223], v239 offset:288
	ds_read_b128 v[224:227], v239 offset:304
	v_lshlrev_b32_e32 v240, 4, v237
	v_sub_u32_e32 v241, 0x7f, v240
	v_sub_u32_e32 v242, 63, v240
	v_mov_b32_e32 v243, 0xffffff80
	s_waitcnt lgkmcnt(7)
	v_ashrrev_i32_e32 v122, 31, v124
	v_or_b32_e32 v122, 0x80000000, v122
	v_xor_b32_e32 v124, v124, v122
	v_and_or_b32 v124, v124, v243, v241
	v_ashrrev_i32_e32 v123, 31, v125
	v_or_b32_e32 v123, 0x80000000, v123
	v_xor_b32_e32 v125, v125, v123
	v_and_or_b32 v125, v125, v243, v241
	v_subrev_u32_e32 v125, 1, v125
	v_ashrrev_i32_e32 v140, 31, v126
	v_or_b32_e32 v140, 0x80000000, v140
	v_xor_b32_e32 v126, v126, v140
	v_and_or_b32 v126, v126, v243, v241
	v_subrev_u32_e32 v126, 2, v126
	v_ashrrev_i32_e32 v141, 31, v127
	v_or_b32_e32 v141, 0x80000000, v141
	v_xor_b32_e32 v127, v127, v141
	v_and_or_b32 v127, v127, v243, v241
	v_subrev_u32_e32 v127, 3, v127
	s_waitcnt lgkmcnt(6)
	v_ashrrev_i32_e32 v142, 31, v128
	v_or_b32_e32 v142, 0x80000000, v142
	v_xor_b32_e32 v128, v128, v142
	v_and_or_b32 v128, v128, v243, v241
	v_subrev_u32_e32 v128, 4, v128
	v_ashrrev_i32_e32 v143, 31, v129
	v_or_b32_e32 v143, 0x80000000, v143
	v_xor_b32_e32 v129, v129, v143
	v_and_or_b32 v129, v129, v243, v241
	v_subrev_u32_e32 v129, 5, v129
	v_ashrrev_i32_e32 v144, 31, v130
	v_or_b32_e32 v144, 0x80000000, v144
	v_xor_b32_e32 v130, v130, v144
	v_and_or_b32 v130, v130, v243, v241
	v_subrev_u32_e32 v130, 6, v130
	v_ashrrev_i32_e32 v145, 31, v131
	v_or_b32_e32 v145, 0x80000000, v145
	v_xor_b32_e32 v131, v131, v145
	v_and_or_b32 v131, v131, v243, v241
	v_subrev_u32_e32 v131, 7, v131
	s_waitcnt lgkmcnt(5)
	v_ashrrev_i32_e32 v194, 31, v132
	v_or_b32_e32 v194, 0x80000000, v194
	v_xor_b32_e32 v132, v132, v194
	v_and_or_b32 v132, v132, v243, v241
	v_subrev_u32_e32 v132, 8, v132
	v_ashrrev_i32_e32 v195, 31, v133
	v_or_b32_e32 v195, 0x80000000, v195
	v_xor_b32_e32 v133, v133, v195
	v_and_or_b32 v133, v133, v243, v241
	v_subrev_u32_e32 v133, 9, v133
	v_ashrrev_i32_e32 v196, 31, v134
	v_or_b32_e32 v196, 0x80000000, v196
	v_xor_b32_e32 v134, v134, v196
	v_and_or_b32 v134, v134, v243, v241
	v_subrev_u32_e32 v134, 10, v134
	v_ashrrev_i32_e32 v197, 31, v135
	v_or_b32_e32 v197, 0x80000000, v197
	v_xor_b32_e32 v135, v135, v197
	v_and_or_b32 v135, v135, v243, v241
	v_subrev_u32_e32 v135, 11, v135
	s_waitcnt lgkmcnt(4)
	v_ashrrev_i32_e32 v198, 31, v136
	v_or_b32_e32 v198, 0x80000000, v198
	v_xor_b32_e32 v136, v136, v198
	v_and_or_b32 v136, v136, v243, v241
	v_subrev_u32_e32 v136, 12, v136
	v_ashrrev_i32_e32 v199, 31, v137
	v_or_b32_e32 v199, 0x80000000, v199
	v_xor_b32_e32 v137, v137, v199
	v_and_or_b32 v137, v137, v243, v241
	v_subrev_u32_e32 v137, 13, v137
	v_ashrrev_i32_e32 v200, 31, v138
	v_or_b32_e32 v200, 0x80000000, v200
	v_xor_b32_e32 v138, v138, v200
	v_and_or_b32 v138, v138, v243, v241
	v_subrev_u32_e32 v138, 14, v138
	v_ashrrev_i32_e32 v201, 31, v139
	v_or_b32_e32 v201, 0x80000000, v201
	v_xor_b32_e32 v139, v139, v201
	v_and_or_b32 v139, v139, v243, v241
	v_subrev_u32_e32 v139, 15, v139
	s_waitcnt lgkmcnt(3)
	v_ashrrev_i32_e32 v202, 31, v212
	v_or_b32_e32 v202, 0x80000000, v202
	v_xor_b32_e32 v212, v212, v202
	v_and_or_b32 v212, v212, v243, v242
	v_ashrrev_i32_e32 v203, 31, v213
	v_or_b32_e32 v203, 0x80000000, v203
	v_xor_b32_e32 v213, v213, v203
	v_and_or_b32 v213, v213, v243, v242
	v_subrev_u32_e32 v213, 1, v213
	v_ashrrev_i32_e32 v204, 31, v214
	v_or_b32_e32 v204, 0x80000000, v204
	v_xor_b32_e32 v214, v214, v204
	v_and_or_b32 v214, v214, v243, v242
	v_subrev_u32_e32 v214, 2, v214
	v_ashrrev_i32_e32 v205, 31, v215
	v_or_b32_e32 v205, 0x80000000, v205
	v_xor_b32_e32 v215, v215, v205
	v_and_or_b32 v215, v215, v243, v242
	v_subrev_u32_e32 v215, 3, v215
	s_waitcnt lgkmcnt(2)
	v_ashrrev_i32_e32 v228, 31, v216
	v_or_b32_e32 v228, 0x80000000, v228
	v_xor_b32_e32 v216, v216, v228
	v_and_or_b32 v216, v216, v243, v242
	v_subrev_u32_e32 v216, 4, v216
	v_ashrrev_i32_e32 v229, 31, v217
	v_or_b32_e32 v229, 0x80000000, v229
	v_xor_b32_e32 v217, v217, v229
	v_and_or_b32 v217, v217, v243, v242
	v_subrev_u32_e32 v217, 5, v217
	v_ashrrev_i32_e32 v230, 31, v218
	v_or_b32_e32 v230, 0x80000000, v230
	v_xor_b32_e32 v218, v218, v230
	v_and_or_b32 v218, v218, v243, v242
	v_subrev_u32_e32 v218, 6, v218
	v_ashrrev_i32_e32 v231, 31, v219
	v_or_b32_e32 v231, 0x80000000, v231
	v_xor_b32_e32 v219, v219, v231
	v_and_or_b32 v219, v219, v243, v242
	v_subrev_u32_e32 v219, 7, v219
	s_waitcnt lgkmcnt(1)
	v_ashrrev_i32_e32 v232, 31, v220
	v_or_b32_e32 v232, 0x80000000, v232
	v_xor_b32_e32 v220, v220, v232
	v_and_or_b32 v220, v220, v243, v242
	v_subrev_u32_e32 v220, 8, v220
	v_ashrrev_i32_e32 v233, 31, v221
	v_or_b32_e32 v233, 0x80000000, v233
	v_xor_b32_e32 v221, v221, v233
	v_and_or_b32 v221, v221, v243, v242
	v_subrev_u32_e32 v221, 9, v221
	v_ashrrev_i32_e32 v234, 31, v222
	v_or_b32_e32 v234, 0x80000000, v234
	v_xor_b32_e32 v222, v222, v234
	v_and_or_b32 v222, v222, v243, v242
	v_subrev_u32_e32 v222, 10, v222
	v_ashrrev_i32_e32 v235, 31, v223
	v_or_b32_e32 v235, 0x80000000, v235
	v_xor_b32_e32 v223, v223, v235
	v_and_or_b32 v223, v223, v243, v242
	v_subrev_u32_e32 v223, 11, v223
	s_waitcnt lgkmcnt(0)
; DI unsigned ordkey(float f) { const unsigned u = __float_as_uint(f); return (u & 0x80000000u) ? ~u : (u | 0x80000000u); }
; #define CE_DESC(x, y) do { const unsigned mx_ = (x) > (y) ? (x) : (y); const unsigned mn_ = (x) > (y) ? (y) : (x); (x) = mx_; (y) = mn_; } while (0)
; DI void sort16_desc(unsigned (&a)[16]) {
; #pragma unroll
;   for (int k = 2; k <= 16; k <<= 1)
; #pragma unroll
;     for (int j = k >> 1; j > 0; j >>= 1)
; #pragma unroll
;       for (int i = 0; i < 16; ++i) {
;         const int l = i ^ j;
;         if (l > i) { if ((i & k) == 0) CE_DESC(a[i], a[l]); else CE_DESC(a[l], a[i]); }
;       }
; }
; DI void peer_select_unit(const Params& p, int unit, char* lds, const bf16x8 (&kb)[4][4]) {
;     ...
;     for (int j = 0; j < 4; ++j) {
;       const f32x4 v = *(const f32x4*)(srow + 4 * j);
; #pragma unroll
;       for (int e = 0; e < 4; ++e) a[4 * j + e] = (ordkey(v[e]) & ~127u) | (unsigned)(127 - (16 * part + 4 * j + e));
;     }
;     sort16_desc(a);
	v_ashrrev_i32_e32 v122, 31, v224
	v_or_b32_e32 v122, 0x80000000, v122
	v_xor_b32_e32 v224, v224, v122
	v_and_or_b32 v224, v224, v243, v242
	v_subrev_u32_e32 v224, 12, v224
	v_ashrrev_i32_e32 v123, 31, v225
	v_or_b32_e32 v123, 0x80000000, v123
	v_xor_b32_e32 v225, v225, v123
	v_and_or_b32 v225, v225, v243, v242
	v_subrev_u32_e32 v225, 13, v225
	v_ashrrev_i32_e32 v140, 31, v226
	v_or_b32_e32 v140, 0x80000000, v140
	v_xor_b32_e32 v226, v226, v140
	v_and_or_b32 v226, v226, v243, v242
	v_subrev_u32_e32 v226, 14, v226
	v_ashrrev_i32_e32 v141, 31, v227
	v_or_b32_e32 v141, 0x80000000, v141
	v_xor_b32_e32 v227, v227, v141
	v_and_or_b32 v227, v227, v243, v242
	v_subrev_u32_e32 v227, 15, v227
	v_max_u32_e32 v142, v124, v125
	v_min_u32_e32 v143, v124, v125
	v_max_u32_e32 v144, v212, v213
	v_min_u32_e32 v145, v212, v213
	v_max_u32_e32 v194, v127, v126
	v_min_u32_e32 v195, v127, v126
	v_max_u32_e32 v196, v215, v214
	v_min_u32_e32 v197, v215, v214
	v_max_u32_e32 v198, v128, v129
	v_min_u32_e32 v199, v128, v129
	v_max_u32_e32 v200, v216, v217
	v_min_u32_e32 v201, v216, v217
	v_max_u32_e32 v202, v131, v130
	v_min_u32_e32 v203, v131, v130
	v_max_u32_e32 v204, v219, v218
	v_min_u32_e32 v205, v219, v218
	v_max_u32_e32 v228, v132, v133
	v_min_u32_e32 v229, v132, v133
	v_max_u32_e32 v230, v220, v221
	v_min_u32_e32 v231, v220, v221
	v_max_u32_e32 v232, v135, v134
	v_min_u32_e32 v233, v135, v134
	v_max_u32_e32 v234, v223, v222
	v_min_u32_e32 v235, v223, v222
	v_max_u32_e32 v122, v136, v137
	v_min_u32_e32 v123, v136, v137
	v_max_u32_e32 v140, v224, v225
	v_min_u32_e32 v141, v224, v225
	v_max_u32_e32 v124, v139, v138
	v_min_u32_e32 v125, v139, v138
	v_max_u32_e32 v212, v227, v226
	v_min_u32_e32 v213, v227, v226
	v_max_u32_e32 v127, v142, v195
	v_min_u32_e32 v126, v142, v195
	v_max_u32_e32 v215, v144, v197
	v_min_u32_e32 v214, v144, v197
	v_max_u32_e32 v128, v143, v194
	v_min_u32_e32 v129, v143, v194
	v_max_u32_e32 v216, v145, v196
	v_min_u32_e32 v217, v145, v196
	v_max_u32_e32 v131, v203, v198
	v_min_u32_e32 v130, v203, v198
	v_max_u32_e32 v219, v205, v200
	v_min_u32_e32 v218, v205, v200
	v_max_u32_e32 v132, v202, v199
	v_min_u32_e32 v133, v202, v199
	v_max_u32_e32 v220, v204, v201
	v_min_u32_e32 v221, v204, v201
	v_max_u32_e32 v135, v228, v233
	v_min_u32_e32 v134, v228, v233
	v_max_u32_e32 v223, v230, v235
	v_min_u32_e32 v222, v230, v235
	v_max_u32_e32 v136, v229, v232
	v_min_u32_e32 v137, v229, v232
	v_max_u32_e32 v224, v231, v234
	v_min_u32_e32 v225, v231, v234
	v_max_u32_e32 v139, v125, v122
	v_min_u32_e32 v138, v125, v122
	v_max_u32_e32 v227, v213, v140
	v_min_u32_e32 v226, v213, v140
	v_max_u32_e32 v142, v124, v123
	v_min_u32_e32 v195, v124, v123
	v_max_u32_e32 v144, v212, v141
	v_min_u32_e32 v197, v212, v141
	v_max_u32_e32 v143, v127, v128
	v_min_u32_e32 v194, v127, v128
	v_max_u32_e32 v145, v215, v216
	v_min_u32_e32 v196, v215, v216
	v_max_u32_e32 v203, v126, v129
	v_min_u32_e32 v198, v126, v129
	v_max_u32_e32 v205, v214, v217
	v_min_u32_e32 v200, v214, v217
	v_max_u32_e32 v202, v133, v130
	v_min_u32_e32 v199, v133, v130
	v_max_u32_e32 v204, v221, v218
	v_min_u32_e32 v201, v221, v218
	v_max_u32_e32 v228, v132, v131
	v_min_u32_e32 v233, v132, v131
	v_max_u32_e32 v230, v220, v219
	v_min_u32_e32 v235, v220, v219
	v_max_u32_e32 v229, v135, v136
	v_min_u32_e32 v232, v135, v136
	v_max_u32_e32 v231, v223, v224
	v_min_u32_e32 v234, v223, v224
	v_max_u32_e32 v125, v134, v137
	v_min_u32_e32 v122, v134, v137
	v_max_u32_e32 v213, v222, v225
	v_min_u32_e32 v140, v222, v225
	v_max_u32_e32 v124, v195, v138
	v_min_u32_e32 v123, v195, v138
	v_max_u32_e32 v212, v197, v226
	v_min_u32_e32 v141, v197, v226
	v_max_u32_e32 v127, v142, v139
	v_min_u32_e32 v128, v142, v139
	v_max_u32_e32 v215, v144, v227
	v_min_u32_e32 v216, v144, v227
	v_max_u32_e32 v126, v143, v199
	v_min_u32_e32 v129, v143, v199
	v_max_u32_e32 v214, v145, v201
	v_min_u32_e32 v217, v145, v201
	v_max_u32_e32 v133, v194, v202
	v_min_u32_e32 v130, v194, v202
	v_max_u32_e32 v221, v196, v204
	v_min_u32_e32 v218, v196, v204
	v_max_u32_e32 v132, v203, v233
	v_min_u32_e32 v131, v203, v233
	v_max_u32_e32 v220, v205, v235
	v_min_u32_e32 v219, v205, v235
	v_max_u32_e32 v135, v198, v228
	v_min_u32_e32 v136, v198, v228
	v_max_u32_e32 v223, v200, v230
	v_min_u32_e32 v224, v200, v230
	v_max_u32_e32 v134, v123, v229
	v_min_u32_e32 v137, v123, v229
	v_max_u32_e32 v222, v141, v231
	v_min_u32_e32 v225, v141, v231
	v_max_u32_e32 v195, v124, v232
	v_min_u32_e32 v138, v124, v232
	v_max_u32_e32 v197, v212, v234
	v_min_u32_e32 v226, v212, v234
	v_max_u32_e32 v142, v128, v125
	v_min_u32_e32 v139, v128, v125
	v_max_u32_e32 v144, v216, v213
	v_min_u32_e32 v227, v216, v213
	v_max_u32_e32 v143, v127, v122
	v_min_u32_e32 v199, v127, v122
	v_max_u32_e32 v145, v215, v140
	v_min_u32_e32 v201, v215, v140
	v_max_u32_e32 v194, v126, v132
	v_min_u32_e32 v202, v126, v132
	v_max_u32_e32 v196, v214, v220
	v_min_u32_e32 v204, v214, v220
	v_max_u32_e32 v203, v133, v135
	v_min_u32_e32 v233, v133, v135
	v_max_u32_e32 v205, v221, v223
	v_min_u32_e32 v235, v221, v223
	v_max_u32_e32 v198, v129, v131
	v_min_u32_e32 v228, v129, v131
	v_max_u32_e32 v200, v217, v219
	v_min_u32_e32 v230, v217, v219
	v_max_u32_e32 v123, v130, v136
	v_min_u32_e32 v229, v130, v136
	v_max_u32_e32 v141, v218, v224
	v_min_u32_e32 v231, v218, v224
	v_max_u32_e32 v124, v139, v137
	v_min_u32_e32 v232, v139, v137
	v_max_u32_e32 v212, v227, v225
	v_min_u32_e32 v234, v227, v225
	v_max_u32_e32 v128, v199, v138
	v_min_u32_e32 v125, v199, v138
	v_max_u32_e32 v216, v201, v226
	v_min_u32_e32 v213, v201, v226
	v_max_u32_e32 v127, v142, v134
	v_min_u32_e32 v122, v142, v134
	v_max_u32_e32 v215, v144, v222
; #define CE_DESC(x, y) do { const unsigned mx_ = (x) > (y) ? (x) : (y); const unsigned mn_ = (x) > (y) ? (y) : (x); (x) = mx_; (y) = mn_; } while (0)
; DI void sort16_desc(unsigned (&a)[16]) {
; #pragma unroll
;   for (int k = 2; k <= 16; k <<= 1)
; #pragma unroll
;     for (int j = k >> 1; j > 0; j >>= 1)
; #pragma unroll
;       for (int i = 0; i < 16; ++i) {
;         const int l = i ^ j;
;         if (l > i) { if ((i & k) == 0) CE_DESC(a[i], a[l]); else CE_DESC(a[l], a[i]); }
;       }
; }
; DI void merge16_desc(unsigned (&a)[16], const unsigned (&b)[16]) {
; #pragma unroll
;   for (int i = 0; i < 16; ++i) a[i] = a[i] > b[15 - i] ? a[i] : b[15 - i];
	v_min_u32_e32 v140, v144, v222
	v_max_u32_e32 v126, v143, v195
	v_min_u32_e32 v132, v143, v195
	v_max_u32_e32 v214, v145, v197
	v_min_u32_e32 v220, v145, v197
	v_max_u32_e32 v133, v194, v203
	v_min_u32_e32 v135, v194, v203
	v_max_u32_e32 v221, v196, v205
	v_min_u32_e32 v223, v196, v205
	v_max_u32_e32 v129, v202, v233
	v_min_u32_e32 v131, v202, v233
	v_max_u32_e32 v217, v204, v235
	v_min_u32_e32 v219, v204, v235
	v_max_u32_e32 v130, v198, v123
	v_min_u32_e32 v136, v198, v123
	v_max_u32_e32 v218, v200, v141
	v_min_u32_e32 v224, v200, v141
	v_max_u32_e32 v139, v228, v229
	v_min_u32_e32 v137, v228, v229
	v_max_u32_e32 v227, v230, v231
	v_min_u32_e32 v225, v230, v231
	v_max_u32_e32 v199, v125, v232
	v_min_u32_e32 v138, v125, v232
	v_max_u32_e32 v201, v213, v234
	v_min_u32_e32 v226, v213, v234
	v_max_u32_e32 v142, v128, v124
	v_min_u32_e32 v134, v128, v124
	v_max_u32_e32 v144, v216, v212
	v_min_u32_e32 v222, v216, v212
	v_max_u32_e32 v143, v132, v122
	v_min_u32_e32 v195, v132, v122
	v_max_u32_e32 v145, v220, v140
	v_min_u32_e32 v197, v220, v140
	v_max_u32_e32 v194, v126, v127
	v_min_u32_e32 v203, v126, v127
	v_max_u32_e32 v196, v214, v215
	v_min_u32_e32 v205, v214, v215
	v_max_u32_e32 v202, v133, v138
	v_min_u32_e32 v233, v133, v138
	v_max_u32_e32 v204, v221, v226
	v_min_u32_e32 v235, v221, v226
	v_max_u32_e32 v198, v135, v199
	v_min_u32_e32 v123, v135, v199
	v_max_u32_e32 v200, v223, v201
	v_min_u32_e32 v141, v223, v201
	v_max_u32_e32 v228, v129, v134
	v_min_u32_e32 v229, v129, v134
	v_max_u32_e32 v230, v217, v222
	v_min_u32_e32 v231, v217, v222
	v_max_u32_e32 v125, v131, v142
	v_min_u32_e32 v232, v131, v142
	v_max_u32_e32 v213, v219, v144
	v_min_u32_e32 v234, v219, v144
	v_max_u32_e32 v128, v130, v195
	v_min_u32_e32 v124, v130, v195
	v_max_u32_e32 v216, v218, v197
	v_min_u32_e32 v212, v218, v197
	v_max_u32_e32 v132, v136, v143
	v_min_u32_e32 v122, v136, v143
	v_max_u32_e32 v220, v224, v145
	v_min_u32_e32 v140, v224, v145
	v_max_u32_e32 v126, v139, v203
	v_min_u32_e32 v127, v139, v203
	v_max_u32_e32 v214, v227, v205
	v_min_u32_e32 v215, v227, v205
	v_max_u32_e32 v133, v137, v194
	v_min_u32_e32 v138, v137, v194
	v_max_u32_e32 v221, v225, v196
	v_min_u32_e32 v226, v225, v196
	v_max_u32_e32 v135, v202, v128
	v_min_u32_e32 v199, v202, v128
	v_max_u32_e32 v223, v204, v216
	v_min_u32_e32 v201, v204, v216
	v_max_u32_e32 v129, v198, v132
	v_min_u32_e32 v134, v198, v132
	v_max_u32_e32 v217, v200, v220
	v_min_u32_e32 v222, v200, v220
	v_max_u32_e32 v131, v228, v126
	v_min_u32_e32 v142, v228, v126
	v_max_u32_e32 v219, v230, v214
	v_min_u32_e32 v144, v230, v214
	v_max_u32_e32 v130, v125, v133
	v_min_u32_e32 v195, v125, v133
	v_max_u32_e32 v218, v213, v221
	v_min_u32_e32 v197, v213, v221
	v_max_u32_e32 v136, v233, v124
	v_min_u32_e32 v143, v233, v124
	v_max_u32_e32 v224, v235, v212
	v_min_u32_e32 v145, v235, v212
	v_max_u32_e32 v139, v123, v122
	v_min_u32_e32 v203, v123, v122
	v_max_u32_e32 v227, v141, v140
	v_min_u32_e32 v205, v141, v140
	v_max_u32_e32 v137, v229, v127
	v_min_u32_e32 v194, v229, v127
	v_max_u32_e32 v225, v231, v215
	v_min_u32_e32 v196, v231, v215
	v_max_u32_e32 v202, v232, v138
	v_min_u32_e32 v128, v232, v138
	v_max_u32_e32 v204, v234, v226
	v_min_u32_e32 v216, v234, v226
	v_max_u32_e32 v198, v135, v131
	v_min_u32_e32 v132, v135, v131
	v_max_u32_e32 v200, v223, v219
	v_min_u32_e32 v220, v223, v219
	v_max_u32_e32 v228, v129, v130
	v_min_u32_e32 v126, v129, v130
	v_max_u32_e32 v230, v217, v218
	v_min_u32_e32 v214, v217, v218
	v_max_u32_e32 v125, v199, v142
	v_min_u32_e32 v133, v199, v142
	v_max_u32_e32 v213, v201, v144
	v_min_u32_e32 v221, v201, v144
	v_max_u32_e32 v233, v134, v195
	v_min_u32_e32 v124, v134, v195
	v_max_u32_e32 v235, v222, v197
	v_min_u32_e32 v212, v222, v197
	v_max_u32_e32 v123, v136, v137
	v_min_u32_e32 v122, v136, v137
	v_max_u32_e32 v141, v224, v225
	v_min_u32_e32 v140, v224, v225
	v_max_u32_e32 v229, v139, v202
	v_min_u32_e32 v127, v139, v202
	v_max_u32_e32 v231, v227, v204
	v_min_u32_e32 v215, v227, v204
	v_max_u32_e32 v232, v143, v194
	v_min_u32_e32 v138, v143, v194
	v_max_u32_e32 v234, v145, v196
	v_min_u32_e32 v226, v145, v196
	v_max_u32_e32 v135, v203, v128
	v_min_u32_e32 v131, v203, v128
	v_max_u32_e32 v223, v205, v216
	v_min_u32_e32 v219, v205, v216
	v_max_u32_e32 v129, v198, v228
	v_min_u32_e32 v130, v198, v228
	v_max_u32_e32 v217, v200, v230
	v_min_u32_e32 v218, v200, v230
	v_max_u32_e32 v199, v132, v126
	v_min_u32_e32 v142, v132, v126
	v_max_u32_e32 v201, v220, v214
	v_min_u32_e32 v144, v220, v214
	v_max_u32_e32 v134, v125, v233
	v_min_u32_e32 v195, v125, v233
	v_max_u32_e32 v222, v213, v235
	v_min_u32_e32 v197, v213, v235
	v_max_u32_e32 v136, v133, v124
	v_min_u32_e32 v137, v133, v124
	v_max_u32_e32 v224, v221, v212
	v_min_u32_e32 v225, v221, v212
	v_max_u32_e32 v139, v123, v229
	v_min_u32_e32 v202, v123, v229
	v_max_u32_e32 v227, v141, v231
	v_min_u32_e32 v204, v141, v231
	v_max_u32_e32 v143, v122, v127
	v_min_u32_e32 v194, v122, v127
	v_max_u32_e32 v145, v140, v215
	v_min_u32_e32 v196, v140, v215
	v_max_u32_e32 v203, v232, v135
	v_min_u32_e32 v128, v232, v135
	v_max_u32_e32 v205, v234, v223
	v_min_u32_e32 v216, v234, v223
	v_max_u32_e32 v198, v138, v131
	v_min_u32_e32 v228, v138, v131
	v_max_u32_e32 v200, v226, v219
	v_min_u32_e32 v230, v226, v219
	v_max_u32_e32 v132, v129, v230
	v_max_u32_e32 v126, v130, v200
	v_max_u32_e32 v220, v199, v216
	v_max_u32_e32 v214, v142, v205
	v_max_u32_e32 v125, v134, v196
	v_max_u32_e32 v233, v195, v145
	v_max_u32_e32 v213, v136, v204
	v_max_u32_e32 v235, v137, v227
	v_max_u32_e32 v133, v139, v225
	v_max_u32_e32 v124, v202, v224
	v_max_u32_e32 v221, v143, v197
; #define CE_DESC(x, y) do { const unsigned mx_ = (x) > (y) ? (x) : (y); const unsigned mn_ = (x) > (y) ? (y) : (x); (x) = mx_; (y) = mn_; } while (0)
; DI void merge16_desc(unsigned (&a)[16], const unsigned (&b)[16]) {
; #pragma unroll
;   for (int i = 0; i < 16; ++i) a[i] = a[i] > b[15 - i] ? a[i] : b[15 - i];
; #pragma unroll
;   for (int j = 8; j > 0; j >>= 1)
; #pragma unroll
;     for (int i = 0; i < 16; ++i) if ((i & j) == 0) CE_DESC(a[i], a[i + j]);
; }
; template <int CTRL> DI void dpp16(unsigned (&b)[16], const unsigned (&a)[16]) {
; #pragma unroll
;   for (int s = 0; s < 16; ++s) b[s] = (unsigned)__builtin_amdgcn_update_dpp(0, (int)a[s], CTRL, 0xF, 0xF, true);
; }
	v_max_u32_e32 v212, v194, v222
	v_max_u32_e32 v123, v203, v144
	v_max_u32_e32 v229, v128, v201
	v_max_u32_e32 v141, v198, v218
	v_max_u32_e32 v231, v228, v217
	v_max_u32_e32 v122, v132, v133
	v_min_u32_e32 v127, v132, v133
	v_max_u32_e32 v140, v126, v124
	v_min_u32_e32 v215, v126, v124
	v_max_u32_e32 v232, v220, v221
	v_min_u32_e32 v135, v220, v221
	v_max_u32_e32 v234, v214, v212
	v_min_u32_e32 v223, v214, v212
	v_max_u32_e32 v138, v125, v123
	v_min_u32_e32 v131, v125, v123
	v_max_u32_e32 v226, v233, v229
	v_min_u32_e32 v219, v233, v229
	v_max_u32_e32 v129, v213, v141
	v_min_u32_e32 v130, v213, v141
	v_max_u32_e32 v199, v235, v231
	v_min_u32_e32 v142, v235, v231
	v_max_u32_e32 v134, v122, v138
	v_min_u32_e32 v195, v122, v138
	v_max_u32_e32 v136, v140, v226
	v_min_u32_e32 v137, v140, v226
	v_max_u32_e32 v139, v232, v129
	v_min_u32_e32 v202, v232, v129
	v_max_u32_e32 v143, v234, v199
	v_min_u32_e32 v194, v234, v199
	v_max_u32_e32 v203, v127, v131
	v_min_u32_e32 v128, v127, v131
	v_max_u32_e32 v198, v215, v219
	v_min_u32_e32 v228, v215, v219
	v_max_u32_e32 v217, v135, v130
	v_min_u32_e32 v218, v135, v130
	v_max_u32_e32 v201, v223, v142
	v_min_u32_e32 v144, v223, v142
	v_max_u32_e32 v222, v134, v139
	v_min_u32_e32 v197, v134, v139
	v_max_u32_e32 v224, v136, v143
	v_min_u32_e32 v225, v136, v143
	v_max_u32_e32 v227, v195, v202
	v_min_u32_e32 v204, v195, v202
	v_max_u32_e32 v145, v137, v194
	v_min_u32_e32 v196, v137, v194
	v_max_u32_e32 v205, v203, v217
	v_min_u32_e32 v216, v203, v217
	v_max_u32_e32 v200, v198, v201
	v_min_u32_e32 v230, v198, v201
	v_max_u32_e32 v132, v128, v218
	v_min_u32_e32 v133, v128, v218
	v_max_u32_e32 v126, v228, v144
	v_min_u32_e32 v124, v228, v144
	v_max_u32_e32 v220, v222, v224
	v_min_u32_e32 v221, v222, v224
	v_max_u32_e32 v214, v197, v225
	v_min_u32_e32 v212, v197, v225
	v_max_u32_e32 v125, v227, v145
	v_min_u32_e32 v123, v227, v145
	v_max_u32_e32 v233, v204, v196
	v_min_u32_e32 v229, v204, v196
	v_max_u32_e32 v213, v205, v200
	v_min_u32_e32 v141, v205, v200
	v_max_u32_e32 v235, v216, v230
	v_min_u32_e32 v231, v216, v230
	v_max_u32_e32 v122, v132, v126
	v_min_u32_e32 v138, v132, v126
	v_max_u32_e32 v140, v133, v124
	v_min_u32_e32 v226, v133, v124
	s_nop 1
	v_max_u32_dpp v232, v226, v220 quad_perm:[1,0,3,2] row_mask:0xf bank_mask:0xf
	v_max_u32_dpp v129, v140, v221 quad_perm:[1,0,3,2] row_mask:0xf bank_mask:0xf
	v_max_u32_dpp v234, v138, v214 quad_perm:[1,0,3,2] row_mask:0xf bank_mask:0xf
	v_max_u32_dpp v199, v122, v212 quad_perm:[1,0,3,2] row_mask:0xf bank_mask:0xf
	v_max_u32_dpp v127, v231, v125 quad_perm:[1,0,3,2] row_mask:0xf bank_mask:0xf
	v_max_u32_dpp v131, v235, v123 quad_perm:[1,0,3,2] row_mask:0xf bank_mask:0xf
	v_max_u32_dpp v215, v141, v233 quad_perm:[1,0,3,2] row_mask:0xf bank_mask:0xf
	v_max_u32_dpp v219, v213, v229 quad_perm:[1,0,3,2] row_mask:0xf bank_mask:0xf
	v_max_u32_dpp v135, v229, v213 quad_perm:[1,0,3,2] row_mask:0xf bank_mask:0xf
	v_max_u32_dpp v130, v233, v141 quad_perm:[1,0,3,2] row_mask:0xf bank_mask:0xf
	v_max_u32_dpp v223, v123, v235 quad_perm:[1,0,3,2] row_mask:0xf bank_mask:0xf
	v_max_u32_dpp v142, v125, v231 quad_perm:[1,0,3,2] row_mask:0xf bank_mask:0xf
	v_max_u32_dpp v134, v212, v122 quad_perm:[1,0,3,2] row_mask:0xf bank_mask:0xf
	v_max_u32_dpp v139, v214, v138 quad_perm:[1,0,3,2] row_mask:0xf bank_mask:0xf
	v_max_u32_dpp v136, v221, v140 quad_perm:[1,0,3,2] row_mask:0xf bank_mask:0xf
	v_max_u32_dpp v143, v220, v226 quad_perm:[1,0,3,2] row_mask:0xf bank_mask:0xf
	v_max_u32_e32 v195, v232, v135
	v_min_u32_e32 v202, v232, v135
	v_max_u32_e32 v137, v129, v130
	v_min_u32_e32 v194, v129, v130
	v_max_u32_e32 v203, v234, v223
	v_min_u32_e32 v217, v234, v223
	v_max_u32_e32 v198, v199, v142
	v_min_u32_e32 v201, v199, v142
	v_max_u32_e32 v128, v127, v134
	v_min_u32_e32 v218, v127, v134
	v_max_u32_e32 v228, v131, v139
	v_min_u32_e32 v144, v131, v139
	v_max_u32_e32 v222, v215, v136
	v_min_u32_e32 v224, v215, v136
	v_max_u32_e32 v197, v219, v143
	v_min_u32_e32 v225, v219, v143
	v_max_u32_e32 v227, v195, v128
	v_min_u32_e32 v145, v195, v128
	v_max_u32_e32 v204, v137, v228
	v_min_u32_e32 v196, v137, v228
	v_max_u32_e32 v205, v203, v222
	v_min_u32_e32 v200, v203, v222
	v_max_u32_e32 v216, v198, v197
	v_min_u32_e32 v230, v198, v197
	v_max_u32_e32 v132, v202, v218
	v_min_u32_e32 v126, v202, v218
	v_max_u32_e32 v133, v194, v144
	v_min_u32_e32 v124, v194, v144
	v_max_u32_e32 v220, v217, v224
	v_min_u32_e32 v221, v217, v224
	v_max_u32_e32 v214, v201, v225
	v_min_u32_e32 v212, v201, v225
	v_max_u32_e32 v125, v227, v205
	v_min_u32_e32 v123, v227, v205
	v_max_u32_e32 v233, v204, v216
	v_min_u32_e32 v229, v204, v216
	v_max_u32_e32 v213, v145, v200
	v_min_u32_e32 v141, v145, v200
	v_max_u32_e32 v235, v196, v230
	v_min_u32_e32 v231, v196, v230
	v_max_u32_e32 v122, v132, v220
	v_min_u32_e32 v138, v132, v220
	v_max_u32_e32 v140, v133, v214
	v_min_u32_e32 v226, v133, v214
	v_max_u32_e32 v232, v126, v221
	v_min_u32_e32 v135, v126, v221
	v_max_u32_e32 v129, v124, v212
	v_min_u32_e32 v130, v124, v212
	v_max_u32_e32 v234, v125, v233
	v_min_u32_e32 v223, v125, v233
	v_max_u32_e32 v199, v123, v229
	v_min_u32_e32 v142, v123, v229
	v_max_u32_e32 v127, v213, v235
	v_min_u32_e32 v134, v213, v235
	v_max_u32_e32 v131, v141, v231
	v_min_u32_e32 v139, v141, v231
	v_max_u32_e32 v215, v122, v140
	v_min_u32_e32 v136, v122, v140
	v_max_u32_e32 v219, v138, v226
	v_min_u32_e32 v143, v138, v226
	v_max_u32_e32 v195, v232, v129
	v_min_u32_e32 v128, v232, v129
	v_max_u32_e32 v137, v135, v130
	v_min_u32_e32 v228, v135, v130
	s_nop 1
	v_max_u32_dpp v203, v228, v234 quad_perm:[2,3,0,1] row_mask:0xf bank_mask:0xf
; #define CE_DESC(x, y) do { const unsigned mx_ = (x) > (y) ? (x) : (y); const unsigned mn_ = (x) > (y) ? (y) : (x); (x) = mx_; (y) = mn_; } while (0)
; DI void merge16_desc(unsigned (&a)[16], const unsigned (&b)[16]) {
; #pragma unroll
;   for (int i = 0; i < 16; ++i) a[i] = a[i] > b[15 - i] ? a[i] : b[15 - i];
; #pragma unroll
;   for (int j = 8; j > 0; j >>= 1)
; #pragma unroll
;     for (int i = 0; i < 16; ++i) if ((i & j) == 0) CE_DESC(a[i], a[i + j]);
; }
; DI void peer_select_unit(const Params& p, int unit, char* lds, const bf16x8 (&kb)[4][4]) {
;     ...
;     dpp16<0xB1>(bq, a); merge16_desc(a, bq);
;     dpp16<0x4E>(bq, a); merge16_desc(a, bq);
;     dpp16<0x141>(bq, a); merge16_desc(a, bq);
; #pragma unroll
;     for (int s = 0; s < 2; ++s) {
;       unsigned k = 0u;
; #pragma unroll
;       for (int q = 0; q < 8; ++q) k = part == q ? a[2 * q + s] : k;
;       const int idx = 127 - (int)(k & 127u);
;       topv[rr * 16 + 2 * part + s] = sc[rr * 132 + idx]; topi[rr * 16 + 2 * part + s] = idx;
;     }
;   }
;   __syncthreads();
	v_max_u32_dpp v222, v137, v223 quad_perm:[2,3,0,1] row_mask:0xf bank_mask:0xf
	v_max_u32_dpp v198, v128, v199 quad_perm:[2,3,0,1] row_mask:0xf bank_mask:0xf
	v_max_u32_dpp v197, v195, v142 quad_perm:[2,3,0,1] row_mask:0xf bank_mask:0xf
	v_max_u32_dpp v202, v143, v127 quad_perm:[2,3,0,1] row_mask:0xf bank_mask:0xf
	v_max_u32_dpp v218, v219, v134 quad_perm:[2,3,0,1] row_mask:0xf bank_mask:0xf
	v_max_u32_dpp v194, v136, v131 quad_perm:[2,3,0,1] row_mask:0xf bank_mask:0xf
	v_max_u32_dpp v144, v215, v139 quad_perm:[2,3,0,1] row_mask:0xf bank_mask:0xf
	v_max_u32_dpp v217, v139, v215 quad_perm:[2,3,0,1] row_mask:0xf bank_mask:0xf
	v_max_u32_dpp v224, v131, v136 quad_perm:[2,3,0,1] row_mask:0xf bank_mask:0xf
	v_max_u32_dpp v201, v134, v219 quad_perm:[2,3,0,1] row_mask:0xf bank_mask:0xf
	v_max_u32_dpp v225, v127, v143 quad_perm:[2,3,0,1] row_mask:0xf bank_mask:0xf
	v_max_u32_dpp v227, v142, v195 quad_perm:[2,3,0,1] row_mask:0xf bank_mask:0xf
	v_max_u32_dpp v205, v199, v128 quad_perm:[2,3,0,1] row_mask:0xf bank_mask:0xf
	v_max_u32_dpp v204, v223, v137 quad_perm:[2,3,0,1] row_mask:0xf bank_mask:0xf
	v_max_u32_dpp v216, v234, v228 quad_perm:[2,3,0,1] row_mask:0xf bank_mask:0xf
	v_max_u32_e32 v145, v203, v217
	v_min_u32_e32 v200, v203, v217
	v_max_u32_e32 v196, v222, v224
	v_min_u32_e32 v230, v222, v224
	v_max_u32_e32 v132, v198, v201
	v_min_u32_e32 v220, v198, v201
	v_max_u32_e32 v133, v197, v225
	v_min_u32_e32 v214, v197, v225
	v_max_u32_e32 v126, v202, v227
	v_min_u32_e32 v221, v202, v227
	v_max_u32_e32 v124, v218, v205
	v_min_u32_e32 v212, v218, v205
	v_max_u32_e32 v125, v194, v204
	v_min_u32_e32 v233, v194, v204
	v_max_u32_e32 v123, v144, v216
	v_min_u32_e32 v229, v144, v216
	v_max_u32_e32 v213, v145, v126
	v_min_u32_e32 v235, v145, v126
	v_max_u32_e32 v141, v196, v124
	v_min_u32_e32 v231, v196, v124
	v_max_u32_e32 v122, v132, v125
	v_min_u32_e32 v140, v132, v125
	v_max_u32_e32 v138, v133, v123
	v_min_u32_e32 v226, v133, v123
	v_max_u32_e32 v232, v200, v221
	v_min_u32_e32 v129, v200, v221
	v_max_u32_e32 v135, v230, v212
	v_min_u32_e32 v130, v230, v212
	v_max_u32_e32 v234, v220, v233
	v_min_u32_e32 v223, v220, v233
	v_max_u32_e32 v199, v214, v229
	v_min_u32_e32 v142, v214, v229
	v_max_u32_e32 v127, v213, v122
	v_min_u32_e32 v134, v213, v122
	v_max_u32_e32 v131, v141, v138
	v_min_u32_e32 v139, v141, v138
	v_max_u32_e32 v215, v235, v140
	v_min_u32_e32 v136, v235, v140
	v_max_u32_e32 v219, v231, v226
	v_min_u32_e32 v143, v231, v226
	v_max_u32_e32 v195, v232, v234
	v_min_u32_e32 v128, v232, v234
	v_max_u32_e32 v137, v135, v199
	v_min_u32_e32 v228, v135, v199
	v_max_u32_e32 v203, v129, v223
	v_min_u32_e32 v217, v129, v223
	v_max_u32_e32 v222, v130, v142
	v_min_u32_e32 v224, v130, v142
	v_max_u32_e32 v198, v127, v131
	v_min_u32_e32 v201, v127, v131
	v_max_u32_e32 v197, v134, v139
	v_min_u32_e32 v225, v134, v139
	v_max_u32_e32 v202, v215, v219
	v_min_u32_e32 v227, v215, v219
	v_max_u32_e32 v218, v136, v143
	v_min_u32_e32 v205, v136, v143
	v_max_u32_e32 v194, v195, v137
	v_min_u32_e32 v204, v195, v137
	v_max_u32_e32 v144, v128, v228
	v_min_u32_e32 v216, v128, v228
	v_max_u32_e32 v145, v203, v222
	v_min_u32_e32 v126, v203, v222
	v_max_u32_e32 v196, v217, v224
	v_min_u32_e32 v124, v217, v224
	v_cmp_eq_u32_e32 vcc, 1, v237
	s_nop 1
	v_cndmask_b32_e32 v132, v198, v202, vcc
	v_cndmask_b32_e32 v125, v201, v227, vcc
	v_cndmask_b32_e32 v133, v197, v218, vcc
	v_cndmask_b32_e32 v123, v225, v205, vcc
	v_cmp_eq_u32_e32 vcc, 2, v237
	s_nop 1
	v_cndmask_b32_e32 v132, v132, v194, vcc
	v_cndmask_b32_e32 v125, v125, v204, vcc
	v_cndmask_b32_e32 v133, v133, v144, vcc
	v_cndmask_b32_e32 v123, v123, v216, vcc
	v_cmp_eq_u32_e32 vcc, 3, v237
	s_nop 1
	v_cndmask_b32_e32 v132, v132, v145, vcc
	v_cndmask_b32_e32 v125, v125, v126, vcc
	v_cndmask_b32_e32 v133, v133, v196, vcc
	v_cndmask_b32_e32 v123, v123, v124, vcc
	v_and_b32_e32 v240, 0x7f, v132
	v_sub_u32_e32 v228, 0x7f, v240
	v_lshl_add_u32 v132, v228, 2, v238
	ds_read_b32 v232, v132
	v_and_b32_e32 v240, 0x7f, v125
	v_sub_u32_e32 v229, 0x7f, v240
	v_lshl_add_u32 v125, v229, 2, v238
	ds_read_b32 v233, v125
	v_and_b32_e32 v240, 0x7f, v133
	v_sub_u32_e32 v230, 0x7f, v240
	v_lshl_add_u32 v133, v230, 2, v238
	ds_read_b32 v234, v133
	v_and_b32_e32 v240, 0x7f, v123
	v_sub_u32_e32 v231, 0x7f, v240
	v_lshl_add_u32 v123, v231, 2, v238
	ds_read_b32 v235, v123
	v_lshlrev_b32_e32 v239, 6, v236
	v_lshl_add_u32 v239, v237, 4, v239
	v_add_u32_e32 v239, v146, v239
	ds_write_b128 v239, v[228:231] offset:37888
	s_waitcnt lgkmcnt(1)
	ds_write_b128 v239, v[232:235] offset:33792
	v_xor_b32_e32 v66, v249, v66
	v_cmp_gt_i32_e32 vcc, s18, v66
	s_waitcnt lgkmcnt(0)
	s_barrier
	s_and_saveexec_b64 s[8:9], vcc
	s_cbranch_execz .LBB0_1651
; DI unsigned ordkey(float f) { const unsigned u = __float_as_uint(f); return (u & 0x80000000u) ? ~u : (u | 0x80000000u); }
; DI void peer_select_unit(const Params& p, int unit, char* lds, const bf16x8 (&kb)[4][4]) {
;     ...
;   if (tid < 128) {
;     const int tok = tid >> 2, q4 = tid & 3;
;     unsigned c[16], bq[16];
; #pragma unroll
;     for (int i = 0; i < 16; ++i) {
;       const unsigned code = PEER_CAND[16 * q4 + i];
;       const float v = topv[tok * 16 + ((code >> 4) & 15)] + topv[(32 + tok) * 16 + (code & 15)];
;       c[i] = code == 0xFFu ? 0u : ((ordkey(v) & ~255u) | (255u - code));
	v_and_b32_e32 v77, 3, v66
	v_lshrrev_b32_e32 v75, 2, v66
	v_lshlrev_b32_e32 v64, 4, v77
	v_and_b32_e32 v80, 0xffff, v244
	v_lshlrev_b32_e32 v66, 6, v75
	v_lshlrev_b32_e32 v76, 4, v75
	v_cmp_eq_u32_e32 vcc, 3, v77
	v_cmp_ne_u32_e64 s[0:1], 3, v77
	v_mov_b32_e32 v82, 0
	v_lshrrev_b32_e32 v67, 2, v80
	v_and_b32_e32 v68, 15, v80
	v_lshrrev_b16_e32 v79, 8, v80
	v_and_b32_e32 v67, 60, v67
	v_lshlrev_b32_e32 v68, 2, v68
	v_lshrrev_b32_e32 v69, 2, v79
	v_and_b32_e32 v78, 15, v79
	v_add3_u32 v67, v146, v67, v66
	v_add3_u32 v68, v146, v68, v66
	v_and_b32_e32 v69, 60, v69
	v_lshlrev_b32_e32 v78, 2, v78
	v_add3_u32 v81, v146, v69, v66
	v_add3_u32 v78, v146, v78, v66
	ds_read_b32 v67, v67 offset:33792
	ds_read_b32 v69, v68 offset:35840
	ds_read_b32 v66, v81 offset:33792
	ds_read_b32 v68, v78 offset:35840
	v_mov_b32_e32 v81, 0
	v_lshlrev_b32_e32 v78, 2, v76
	v_mov_b32_e32 v83, 0
	v_mov_b32_e32 v84, 0
	v_mov_b32_e32 v85, 0
	v_mov_b32_e32 v86, 0
	v_mov_b32_e32 v87, 0
	v_mov_b32_e32 v88, 0
	v_mov_b32_e32 v89, 0
	v_mov_b32_e32 v90, 0
	v_mov_b32_e32 v91, 0
	v_mov_b32_e32 v92, 0
	v_mov_b32_e32 v93, 0
	v_mov_b32_e32 v94, 0
	s_and_saveexec_b64 s[6:7], s[0:1]
	v_bfe_u32 v82, v244, 16, 8
	v_lshrrev_b32_e32 v238, 2, v82
	v_and_b32_e32 v239, 15, v82
	v_and_b32_e32 v238, 60, v238
	v_lshlrev_b32_e32 v239, 2, v239
	v_add3_u32 v238, v146, v238, v78
	v_add3_u32 v239, v146, v239, v78
	ds_read_b32 v210, v238 offset:33792
	ds_read_b32 v211, v239 offset:35840
	v_bfe_u32 v81, v244, 24, 8
	v_lshrrev_b32_e32 v238, 2, v81
	v_and_b32_e32 v239, 15, v81
	v_and_b32_e32 v238, 60, v238
	v_lshlrev_b32_e32 v239, 2, v239
	v_add3_u32 v238, v146, v238, v78
	v_add3_u32 v239, v146, v239, v78
	ds_read_b32 v212, v238 offset:33792
	ds_read_b32 v213, v239 offset:35840
	v_bfe_u32 v84, v245, 0, 8
	v_lshrrev_b32_e32 v238, 2, v84
	v_and_b32_e32 v239, 15, v84
	v_and_b32_e32 v238, 60, v238
	v_lshlrev_b32_e32 v239, 2, v239
	v_add3_u32 v238, v146, v238, v78
	v_add3_u32 v239, v146, v239, v78
	ds_read_b32 v214, v238 offset:33792
	ds_read_b32 v215, v239 offset:35840
	v_bfe_u32 v83, v245, 8, 8
	v_lshrrev_b32_e32 v238, 2, v83
	v_and_b32_e32 v239, 15, v83
	v_and_b32_e32 v238, 60, v238
	v_lshlrev_b32_e32 v239, 2, v239
	v_add3_u32 v238, v146, v238, v78
	v_add3_u32 v239, v146, v239, v78
	ds_read_b32 v216, v238 offset:33792
	ds_read_b32 v217, v239 offset:35840
	v_bfe_u32 v86, v245, 16, 8
	v_lshrrev_b32_e32 v238, 2, v86
	v_and_b32_e32 v239, 15, v86
	v_and_b32_e32 v238, 60, v238
	v_lshlrev_b32_e32 v239, 2, v239
	v_add3_u32 v238, v146, v238, v78
	v_add3_u32 v239, v146, v239, v78
	ds_read_b32 v218, v238 offset:33792
	ds_read_b32 v219, v239 offset:35840
	v_bfe_u32 v85, v245, 24, 8
	v_lshrrev_b32_e32 v238, 2, v85
	v_and_b32_e32 v239, 15, v85
	v_and_b32_e32 v238, 60, v238
	v_lshlrev_b32_e32 v239, 2, v239
	v_add3_u32 v238, v146, v238, v78
	v_add3_u32 v239, v146, v239, v78
	ds_read_b32 v220, v238 offset:33792
	ds_read_b32 v221, v239 offset:35840
	v_bfe_u32 v88, v246, 0, 8
	v_lshrrev_b32_e32 v238, 2, v88
	v_and_b32_e32 v239, 15, v88
	v_and_b32_e32 v238, 60, v238
	v_lshlrev_b32_e32 v239, 2, v239
	v_add3_u32 v238, v146, v238, v78
	v_add3_u32 v239, v146, v239, v78
	ds_read_b32 v222, v238 offset:33792
	ds_read_b32 v223, v239 offset:35840
	v_bfe_u32 v87, v246, 8, 8
	v_lshrrev_b32_e32 v238, 2, v87
	v_and_b32_e32 v239, 15, v87
	v_and_b32_e32 v238, 60, v238
	v_lshlrev_b32_e32 v239, 2, v239
	v_add3_u32 v238, v146, v238, v78
	v_add3_u32 v239, v146, v239, v78
	ds_read_b32 v224, v238 offset:33792
	ds_read_b32 v225, v239 offset:35840
	v_bfe_u32 v90, v246, 16, 8
	v_lshrrev_b32_e32 v238, 2, v90
	v_and_b32_e32 v239, 15, v90
	v_and_b32_e32 v238, 60, v238
	v_lshlrev_b32_e32 v239, 2, v239
	v_add3_u32 v238, v146, v238, v78
	v_add3_u32 v239, v146, v239, v78
	ds_read_b32 v226, v238 offset:33792
	ds_read_b32 v227, v239 offset:35840
	v_bfe_u32 v89, v246, 24, 8
	v_lshrrev_b32_e32 v238, 2, v89
	v_and_b32_e32 v239, 15, v89
	v_and_b32_e32 v238, 60, v238
	v_lshlrev_b32_e32 v239, 2, v239
	v_add3_u32 v238, v146, v238, v78
	v_add3_u32 v239, v146, v239, v78
	ds_read_b32 v228, v238 offset:33792
	ds_read_b32 v229, v239 offset:35840
	v_bfe_u32 v92, v247, 0, 8
	v_lshrrev_b32_e32 v238, 2, v92
	v_and_b32_e32 v239, 15, v92
	v_and_b32_e32 v238, 60, v238
	v_lshlrev_b32_e32 v239, 2, v239
	v_add3_u32 v238, v146, v238, v78
	v_add3_u32 v239, v146, v239, v78
	ds_read_b32 v230, v238 offset:33792
	ds_read_b32 v231, v239 offset:35840
	v_bfe_u32 v91, v247, 8, 8
	v_lshrrev_b32_e32 v238, 2, v91
	v_and_b32_e32 v239, 15, v91
	v_and_b32_e32 v238, 60, v238
	v_lshlrev_b32_e32 v239, 2, v239
	v_add3_u32 v238, v146, v238, v78
	v_add3_u32 v239, v146, v239, v78
	ds_read_b32 v232, v238 offset:33792
	ds_read_b32 v233, v239 offset:35840
	v_bfe_u32 v94, v247, 16, 8
	v_lshrrev_b32_e32 v238, 2, v94
	v_and_b32_e32 v239, 15, v94
	v_and_b32_e32 v238, 60, v238
	v_lshlrev_b32_e32 v239, 2, v239
	v_add3_u32 v238, v146, v238, v78
	v_add3_u32 v239, v146, v239, v78
	ds_read_b32 v234, v238 offset:33792
	ds_read_b32 v235, v239 offset:35840
	v_bfe_u32 v70, v247, 24, 8
	v_lshrrev_b32_e32 v238, 2, v70
	v_and_b32_e32 v239, 15, v70
	v_and_b32_e32 v238, 60, v238
	v_lshlrev_b32_e32 v239, 2, v239
	v_add3_u32 v238, v146, v238, v78
	v_add3_u32 v239, v146, v239, v78
	ds_read_b32 v236, v238 offset:33792
	ds_read_b32 v237, v239 offset:35840
	s_waitcnt lgkmcnt(0)
; DI unsigned ordkey(float f) { const unsigned u = __float_as_uint(f); return (u & 0x80000000u) ? ~u : (u | 0x80000000u); }
; DI void peer_select_unit(const Params& p, int unit, char* lds, const bf16x8 (&kb)[4][4]) {
;     ...
; #pragma unroll
;     for (int i = 0; i < 16; ++i) {
;       const unsigned code = PEER_CAND[16 * q4 + i];
;       const float v = topv[tok * 16 + ((code >> 4) & 15)] + topv[(32 + tok) * 16 + (code & 15)];
;       c[i] = code == 0xFFu ? 0u : ((ordkey(v) & ~255u) | (255u - code));
	v_add_f32_e32 v210, v210, v211
	v_cmp_gt_i32_e64 s[4:5], 0, v210
	v_not_b32_e32 v211, v210
	v_or_b32_e32 v238, 0x80000000, v210
	v_cndmask_b32_e64 v210, v238, v211, s[4:5]
	v_and_b32_e32 v210, 0xffffff00, v210
	v_bitop3_b32 v82, v210, s19, v82 bitop3:0x36
	v_add_f32_e32 v212, v212, v213
	v_cmp_gt_i32_e64 s[4:5], 0, v212
	v_not_b32_e32 v213, v212
	v_or_b32_e32 v238, 0x80000000, v212
	v_cndmask_b32_e64 v212, v238, v213, s[4:5]
	v_and_b32_e32 v212, 0xffffff00, v212
	v_bitop3_b32 v81, v212, s19, v81 bitop3:0x36
	v_add_f32_e32 v214, v214, v215
	v_cmp_gt_i32_e64 s[4:5], 0, v214
	v_not_b32_e32 v215, v214
	v_or_b32_e32 v238, 0x80000000, v214
	v_cndmask_b32_e64 v214, v238, v215, s[4:5]
	v_and_b32_e32 v214, 0xffffff00, v214
	v_bitop3_b32 v84, v214, s19, v84 bitop3:0x36
	v_add_f32_e32 v216, v216, v217
	v_cmp_gt_i32_e64 s[4:5], 0, v216
	v_not_b32_e32 v217, v216
	v_or_b32_e32 v238, 0x80000000, v216
	v_cndmask_b32_e64 v216, v238, v217, s[4:5]
	v_and_b32_e32 v216, 0xffffff00, v216
	v_bitop3_b32 v83, v216, s19, v83 bitop3:0x36
	v_add_f32_e32 v218, v218, v219
	v_cmp_gt_i32_e64 s[4:5], 0, v218
	v_not_b32_e32 v219, v218
	v_or_b32_e32 v238, 0x80000000, v218
	v_cndmask_b32_e64 v218, v238, v219, s[4:5]
	v_and_b32_e32 v218, 0xffffff00, v218
	v_bitop3_b32 v86, v218, s19, v86 bitop3:0x36
	v_add_f32_e32 v220, v220, v221
	v_cmp_gt_i32_e64 s[4:5], 0, v220
	v_not_b32_e32 v221, v220
	v_or_b32_e32 v238, 0x80000000, v220
	v_cndmask_b32_e64 v220, v238, v221, s[4:5]
	v_and_b32_e32 v220, 0xffffff00, v220
	v_bitop3_b32 v85, v220, s19, v85 bitop3:0x36
	v_add_f32_e32 v222, v222, v223
	v_cmp_gt_i32_e64 s[4:5], 0, v222
	v_not_b32_e32 v223, v222
	v_or_b32_e32 v238, 0x80000000, v222
	v_cndmask_b32_e64 v222, v238, v223, s[4:5]
	v_and_b32_e32 v222, 0xffffff00, v222
	v_bitop3_b32 v88, v222, s19, v88 bitop3:0x36
	v_add_f32_e32 v224, v224, v225
	v_cmp_gt_i32_e64 s[4:5], 0, v224
	v_not_b32_e32 v225, v224
	v_or_b32_e32 v238, 0x80000000, v224
	v_cndmask_b32_e64 v224, v238, v225, s[4:5]
	v_and_b32_e32 v224, 0xffffff00, v224
	v_bitop3_b32 v87, v224, s19, v87 bitop3:0x36
	v_add_f32_e32 v226, v226, v227
	v_cmp_gt_i32_e64 s[4:5], 0, v226
	v_not_b32_e32 v227, v226
	v_or_b32_e32 v238, 0x80000000, v226
	v_cndmask_b32_e64 v226, v238, v227, s[4:5]
	v_and_b32_e32 v226, 0xffffff00, v226
	v_bitop3_b32 v90, v226, s19, v90 bitop3:0x36
	v_add_f32_e32 v228, v228, v229
	v_cmp_gt_i32_e64 s[4:5], 0, v228
	v_not_b32_e32 v229, v228
	v_or_b32_e32 v238, 0x80000000, v228
	v_cndmask_b32_e64 v228, v238, v229, s[4:5]
	v_and_b32_e32 v228, 0xffffff00, v228
	v_bitop3_b32 v89, v228, s19, v89 bitop3:0x36
	v_add_f32_e32 v230, v230, v231
	v_cmp_gt_i32_e64 s[4:5], 0, v230
	v_not_b32_e32 v231, v230
	v_or_b32_e32 v238, 0x80000000, v230
	v_cndmask_b32_e64 v230, v238, v231, s[4:5]
	v_and_b32_e32 v230, 0xffffff00, v230
	v_bitop3_b32 v92, v230, s19, v92 bitop3:0x36
	v_add_f32_e32 v232, v232, v233
	v_cmp_gt_i32_e64 s[4:5], 0, v232
	v_not_b32_e32 v233, v232
	v_or_b32_e32 v238, 0x80000000, v232
	v_cndmask_b32_e64 v232, v238, v233, s[4:5]
	v_and_b32_e32 v232, 0xffffff00, v232
	v_bitop3_b32 v91, v232, s19, v91 bitop3:0x36
	v_add_f32_e32 v234, v234, v235
	v_cmp_gt_i32_e64 s[4:5], 0, v234
	v_not_b32_e32 v235, v234
	v_or_b32_e32 v238, 0x80000000, v234
	v_cndmask_b32_e64 v234, v238, v235, s[4:5]
	v_and_b32_e32 v234, 0xffffff00, v234
	v_bitop3_b32 v94, v234, s19, v94 bitop3:0x36
	v_add_f32_e32 v236, v236, v237
	v_cmp_gt_i32_e64 s[4:5], 0, v236
	v_not_b32_e32 v237, v236
	v_or_b32_e32 v238, 0x80000000, v236
	v_cndmask_b32_e64 v236, v238, v237, s[4:5]
	v_and_b32_e32 v236, 0xffffff00, v236
	v_bitop3_b32 v93, v236, s19, v70 bitop3:0x36
	s_or_b64 exec, exec, s[6:7]
	s_mov_b64 s[4:5], exec
	s_branch .LBB0_1650
